# v22: v21 + byte-phase pin: phase-10 GEMM code shifted 4 bytes so its K-loop head sits at 4 mod 8 like phase 9's (x4 probe: 5120 vs 5144 us)
# baseline (speedup 1.0000x reference)
.LBB0_1504:
	s_cmp_lt_i32 s52, 11
	s_cselect_b64 s[0:1], -1, 0
	s_cmp_gt_i32 s53, 10
	s_cselect_b64 s[2:3], -1, 0
	s_and_b64 s[0:1], s[0:1], s[2:3]
	s_andn2_b64 vcc, exec, s[0:1]
	s_cbranch_vccnz .LBB0_1616
	s_nop 0
	s_waitcnt vmcnt(0)
	v_mov_b32_e32 v3, v0
	s_nop 0
	v_cmp_gt_i32_e32 vcc, 64, v3
	s_and_saveexec_b64 s[0:1], vcc
	s_cbranch_execz .LBB0_1522
	v_and_b32_e32 v1, 31, v3
	v_lshlrev_b32_e32 v4, 2, v1
	v_mov_b32_e32 v5, 0
	v_lshl_add_u64 v[4:5], s[96:97], 0, v[4:5]
	v_add_co_u32_e32 v4, vcc, 0xc000, v4
	s_nop 1
	v_addc_co_u32_e32 v5, vcc, 0, v5, vcc
	global_load_dword v2, v[4:5], off sc1
	v_mbcnt_lo_u32_b32 v4, -1, 0
	v_mbcnt_hi_u32_b32 v5, -1, v4
	v_and_b32_e32 v6, 0x60, v5
	v_add_u32_e32 v4, -1, v5
	v_cmp_lt_i32_e32 vcc, v4, v6
	v_add_u32_e32 v7, -2, v5
	v_add_u32_e32 v8, -4, v5
	v_cndmask_b32_e32 v4, v4, v5, vcc
	v_lshlrev_b32_e32 v10, 2, v4
	v_cmp_lt_i32_e32 vcc, v7, v6
	v_add_u32_e32 v9, -8, v5
	s_waitcnt vmcnt(0)
	v_add_u32_e32 v4, 0xff, v2
	v_ashrrev_i32_e32 v2, 31, v4
	v_add_u32_sdwa v2, v4, v2 dst_sel:DWORD dst_unused:UNUSED_PAD src0_sel:DWORD src1_sel:BYTE_3
	v_ashrrev_i32_e32 v2, 8, v2
	ds_bpermute_b32 v10, v10, v2
	v_cndmask_b32_e32 v7, v7, v5, vcc
	v_cmp_ne_u32_e32 vcc, 0, v1
	v_lshlrev_b32_e32 v7, 2, v7
	s_waitcnt lgkmcnt(0)
	v_cndmask_b32_e32 v10, 0, v10, vcc
	v_add_u32_e32 v10, v10, v2
	ds_bpermute_b32 v7, v7, v10
	v_cmp_lt_i32_e32 vcc, v8, v6
	s_nop 1
	v_cndmask_b32_e32 v8, v8, v5, vcc
	v_cmp_lt_u32_e32 vcc, 1, v1
	v_lshlrev_b32_e32 v8, 2, v8
	s_waitcnt lgkmcnt(0)
	v_cndmask_b32_e32 v7, 0, v7, vcc
	v_add_u32_e32 v7, v7, v10
	ds_bpermute_b32 v8, v8, v7
	v_cmp_lt_i32_e32 vcc, v9, v6
	s_nop 1
	v_cndmask_b32_e32 v9, v9, v5, vcc
	v_cmp_lt_u32_e32 vcc, 3, v1
	v_lshlrev_b32_e32 v9, 2, v9
	s_waitcnt lgkmcnt(0)
	v_cndmask_b32_e32 v8, 0, v8, vcc
	v_add_u32_e32 v7, v8, v7
	ds_bpermute_b32 v8, v9, v7
	v_add_u32_e32 v9, -16, v5
	v_cmp_lt_i32_e32 vcc, v9, v6
	s_nop 1
	v_cndmask_b32_e32 v6, v9, v5, vcc
	v_cmp_lt_u32_e32 vcc, 7, v1
	v_lshlrev_b32_e32 v6, 2, v6
	s_waitcnt lgkmcnt(0)
	v_cndmask_b32_e32 v5, 0, v8, vcc
	v_add_u32_e32 v5, v5, v7
	ds_bpermute_b32 v6, v6, v5
	v_cmp_gt_i32_e32 vcc, 32, v3
	s_and_b64 exec, exec, vcc
	s_cbranch_execz .LBB0_1522
	v_cmp_lt_u32_e32 vcc, 15, v1
	v_lshl_add_u32 v7, v1, 2, 0
	v_add_u32_e32 v7, 0x21000, v7
	s_waitcnt lgkmcnt(0)
	v_cndmask_b32_e32 v3, 0, v6, vcc
	v_add_u32_e32 v5, v3, v5
	v_sub_u32_e32 v3, v5, v2
	v_lshlrev_b32_e32 v6, 8, v3
	v_cmp_eq_u32_e32 vcc, 31, v1
	ds_write_b32 v7, v6
	s_and_saveexec_b64 s[2:3], vcc
	s_add_i32 s4, 0, 0x21080
	v_lshlrev_b32_e32 v5, 8, v5
	v_mov_b32_e32 v6, s4
	ds_write_b32 v6, v5
	s_or_b64 exec, exec, s[2:3]
	s_movk_i32 s2, 0xff
	v_cmp_lt_i32_e32 vcc, s2, v4
	s_and_b64 exec, exec, vcc
	s_cbranch_execz .LBB0_1522
	v_cmp_lt_u32_e32 vcc, 1, v2
	s_mov_b64 s[4:5], -1
	v_mov_b32_e32 v4, 0
	s_and_saveexec_b64 s[2:3], vcc
	s_cbranch_execz .LBB0_1519
	v_add_u32_e32 v5, -2, v2
	v_lshrrev_b32_e32 v4, 1, v5
	v_add_u32_e32 v4, 1, v4
	v_cmp_lt_u32_e32 vcc, 13, v5
	v_mov_b32_e32 v7, 0
	s_and_saveexec_b64 s[4:5], vcc
	s_cbranch_execz .LBB0_1515
	v_lshl_add_u32 v6, v3, 2, 0
	v_and_b32_e32 v5, -8, v4
	s_mov_b32 s8, 0
	v_add_u32_e32 v6, 0x20000, v6
	s_mov_b64 s[6:7], 0

.LBB0_1616:
	s_cmp_lt_i32 s52, 12
	s_cselect_b64 s[0:1], -1, 0
	s_cmp_gt_i32 s53, 11
	s_cselect_b64 s[2:3], -1, 0
	s_and_b64 s[0:1], s[0:1], s[2:3]
	s_andn2_b64 vcc, exec, s[0:1]
	s_cbranch_vccnz .LBB0_1674
	s_nop 0
	v_readlane_b32 s12, v254, 0
	v_ashrrev_i32_e32 v1, 31, v0
	s_waitcnt vmcnt(0)
	v_lshlrev_b64 v[2:3], 2, v[0:1]
	v_readlane_b32 s14, v254, 2
	v_readlane_b32 s15, v254, 3
	v_readlane_b32 s16, v254, 4
	v_readlane_b32 s17, v254, 5
	v_lshl_add_u64 v[4:5], s[14:15], 0, v[2:3]
	v_ashrrev_i32_e32 v64, 6, v0
	v_lshl_add_u64 v[2:3], s[16:17], 0, v[2:3]
	global_load_dword v1, v[4:5], off
	global_load_dword v6, v[4:5], off offset:2048
	global_load_dword v7, v[2:3], off
	global_load_dword v8, v[2:3], off offset:2048
	v_add_co_u32_e32 v4, vcc, 0x1000, v4
	s_mov_b32 s0, 0x8000
	s_nop 0
	v_addc_co_u32_e32 v5, vcc, 0, v5, vcc
	v_add_co_u32_e32 v2, vcc, 0x1000, v2
	v_lshl_add_u32 v76, s72, 3, v64
	s_nop 0
	v_addc_co_u32_e32 v3, vcc, 0, v3, vcc
	global_load_dword v9, v[4:5], off
	global_load_dword v10, v[4:5], off offset:2048
	global_load_dword v11, v[2:3], off
	global_load_dword v12, v[2:3], off offset:2048
	v_lshl_add_u32 v2, v0, 2, 0
	v_and_b32_e32 v0, 63, v0
	v_readlane_b32 s18, v254, 6
	v_readlane_b32 s19, v254, 7
	v_lshl_add_u32 v60, v0, 4, 0
	v_cmp_gt_i32_e32 vcc, s0, v76
	v_readlane_b32 s13, v254, 1
	s_waitcnt vmcnt(0)
	ds_write2st64_b32 v2, v1, v6 offset1:8
	ds_write2st64_b32 v2, v7, v8 offset0:32 offset1:40
	ds_write2st64_b32 v2, v9, v10 offset0:16 offset1:24
	ds_write2st64_b32 v2, v11, v12 offset0:48 offset1:56
	s_waitcnt lgkmcnt(0)
	s_barrier
	s_and_saveexec_b64 s[0:1], vcc
	s_cbranch_execz .LBB0_1620
	s_load_dword s10, s[74:75], 0xf8
	v_lshlrev_b32_e32 v66, 2, v0
	v_lshlrev_b32_e32 v78, 3, v0
	ds_read_b128 v[0:3], v60
	ds_read_b128 v[4:7], v60 offset:1024
	ds_read_b128 v[8:11], v60 offset:8192
	ds_read_b128 v[12:15], v60 offset:9216
	ds_read_b128 v[16:19], v60 offset:2048
	ds_read_b128 v[20:23], v60 offset:3072
	ds_read_b128 v[24:27], v60 offset:10240
	ds_read_b128 v[28:31], v60 offset:11264
	ds_read_b128 v[32:35], v60 offset:4096
	ds_read_b128 v[36:39], v60 offset:5120
	ds_read_b128 v[40:43], v60 offset:12288
	ds_read_b128 v[44:47], v60 offset:13312
	ds_read_b128 v[48:51], v60 offset:6144
	ds_read_b128 v[52:55], v60 offset:7168
	ds_read_b128 v[56:59], v60 offset:14336
	ds_read_b128 v[60:63], v60 offset:15360
	s_add_u32 s2, s96, 0x6de70000
	s_addc_u32 s3, s97, 0
	s_add_u32 s4, s96, 0x6ddf0000
	s_addc_u32 s5, s97, 0
	s_add_u32 s6, s96, 0x6df78000
	v_mov_b32_e32 v79, 0
	s_addc_u32 s7, s97, 0
	v_lshl_add_u64 v[68:69], s[96:97], 0, v[78:79]
	s_mov_b64 s[8:9], 0x5dd70000
	v_lshlrev_b32_e32 v64, 2, v64
	s_waitcnt lgkmcnt(0)
	s_lshl_b32 s13, s10, 3
	v_lshl_add_u64 v[80:81], s[6:7], 0, v[78:79]
	v_or_b32_e32 v82, 0x100, v66
	v_or_b32_e32 v84, 0x200, v66
	v_or_b32_e32 v86, 0x300, v66
	v_or_b32_e32 v88, 0x400, v66
	v_or_b32_e32 v90, 0x500, v66
	v_or_b32_e32 v92, 0x600, v66
	v_or_b32_e32 v94, 0x700, v66
	v_lshl_add_u64 v[96:97], v[68:69], 0, s[8:9]
	v_lshl_add_u32 v98, s72, 5, v64
	s_lshl_b32 s14, s10, 5
	s_mov_b64 s[8:9], 0
	s_mov_b64 s[10:11], 0x1a000
	v_lshlrev_b32_e32 v78, 2, v66
	s_mov_b32 s12, 0x3f9837f0
	v_mov_b32_e32 v83, 0x3727c5ac
	s_mov_b32 s15, 0x800000
	s_movk_i32 s16, 0x7fff
